# v13
# speedup vs baseline: 1.0193x; 1.0039x over previous
.LBB0_78:
	s_or_b64 exec, exec, s[4:5]
	s_waitcnt lgkmcnt(0)
	s_barrier
	s_and_saveexec_b64 s[4:5], s[10:11]
	s_cbranch_execz .LBB0_81
	v_mov_b32_e32 v1, 0x23440
	v_mov_b32_e32 v6, 0x23450
	ds_read_b128 v[2:5], v1
	ds_read_b128 v[6:9], v6
	v_mov_b32_e32 v1, 0x23460
	ds_read_b128 v[10:13], v1
	s_mov_b32 s3, 0x3fb8aa3b
	s_waitcnt lgkmcnt(2)
	v_add_f32_e32 v1, s6, v2
	v_mov_b32_e32 v2, 0x23470
	ds_read_b128 v[14:17], v2
	v_mov_b32_e32 v2, 0x23480
	s_waitcnt lgkmcnt(2)
	v_add_f32_e32 v1, v1, v6
	v_mov_b32_e32 v6, 0x23490
	ds_read_b128 v[18:21], v2
	ds_read_b128 v[22:25], v6
	v_mov_b32_e32 v2, 0x234a0
	v_mov_b32_e32 v6, 0x234b0
	ds_read_b128 v[26:29], v2
	ds_read_b128 v[30:33], v6
	v_add_f32_e32 v2, s6, v3
	v_add_f32_e32 v2, v2, v7
	s_waitcnt lgkmcnt(5)
	v_add_f32_e32 v2, v2, v11
	s_waitcnt lgkmcnt(4)
	v_add_f32_e32 v2, v2, v15
	s_waitcnt lgkmcnt(3)
	v_add_f32_e32 v2, v2, v19
	s_waitcnt lgkmcnt(2)
	v_add_f32_e32 v2, v2, v23
	s_waitcnt lgkmcnt(1)
	v_add_f32_e32 v2, v2, v27
	s_waitcnt lgkmcnt(0)
	v_add_f32_e32 v3, v2, v31
	v_add_f32_e32 v2, s6, v4
	v_add_f32_e32 v2, v2, v8
	v_add_f32_e32 v2, v2, v12
	v_add_f32_e32 v2, v2, v16
	v_add_f32_e32 v2, v2, v20
	v_add_f32_e32 v2, v2, v24
	v_add_f32_e32 v2, v2, v28
	v_add_f32_e32 v6, v2, v32
	v_add_f32_e32 v2, s6, v5
	v_add_f32_e32 v2, v2, v9
	v_add_f32_e32 v2, v2, v13
	v_add_f32_e32 v1, v1, v10
	v_add_f32_e32 v2, v2, v17
	v_add_f32_e32 v1, v1, v14
	v_add_f32_e32 v2, v2, v21
	v_add_f32_e32 v1, v1, v18
	v_add_f32_e32 v2, v2, v25
	v_add_f32_e32 v1, v1, v22
	v_add_f32_e32 v2, v2, v29
	v_add_f32_e32 v1, v1, v26
	v_add_f32_e32 v10, v2, v33
	v_add_f32_e32 v1, v1, v30
	v_max_f32_e32 v2, v6, v10
	v_max3_f32 v2, v1, v3, v2
	v_sub_f32_e32 v1, v1, v2
	v_mul_f32_e32 v4, 0x3fb8aa3b, v1
	v_fma_f32 v5, v1, s3, -v4
	v_rndne_f32_e32 v7, v4
	v_fmac_f32_e32 v5, 0x32a5705f, v1
	v_sub_f32_e32 v4, v4, v7
	v_add_f32_e32 v4, v4, v5
	v_exp_f32_e32 v4, v4
	v_cvt_i32_f32_e32 v5, v7
	v_sub_f32_e32 v3, v3, v2
	v_mul_f32_e32 v12, 0x3fb8aa3b, v3
	s_mov_b32 s4, 0xc2ce8ed0
	v_fma_f32 v13, v3, s3, -v12
	v_rndne_f32_e32 v14, v12
	v_add_u32_e32 v8, 0x22c00, v130
	v_ldexp_f32 v4, v4, v5
	v_cmp_ngt_f32_e32 vcc, s4, v1
	v_fmac_f32_e32 v13, 0x32a5705f, v3
	v_sub_f32_e32 v12, v12, v14
	v_cndmask_b32_e32 v9, 0, v4, vcc
	ds_read2st64_b32 v[4:5], v8 offset1:2
	v_add_f32_e32 v12, v12, v13
	v_exp_f32_e32 v12, v12
	v_cvt_i32_f32_e32 v13, v14
	s_mov_b32 s5, 0x42b17218
	v_mov_b32_e32 v11, 0x7f800000
	v_cmp_nlt_f32_e32 vcc, s5, v1
	v_sub_f32_e32 v6, v6, v2
	v_mov_b32_e32 v7, 0
	v_cndmask_b32_e32 v1, v11, v9, vcc
	v_mul_f32_e32 v9, 0x3fb8aa3b, v6
	s_waitcnt lgkmcnt(0)
	v_fma_f32 v14, v1, v4, 0
	v_ldexp_f32 v4, v12, v13
	v_fma_f32 v12, v6, s3, -v9
	v_rndne_f32_e32 v13, v9
	v_fmac_f32_e32 v12, 0x32a5705f, v6
	v_sub_f32_e32 v9, v9, v13
	v_cmp_ngt_f32_e32 vcc, s4, v3
	v_add_f32_e32 v9, v9, v12
	v_exp_f32_e32 v9, v9
	v_cndmask_b32_e32 v4, 0, v4, vcc
	v_cvt_i32_f32_e32 v12, v13
	v_cmp_nlt_f32_e32 vcc, s5, v3
	s_nop 1
	v_cndmask_b32_e32 v3, v11, v4, vcc
	v_fmac_f32_e32 v14, v3, v5
	v_sub_f32_e32 v5, v10, v2
	v_mul_f32_e32 v10, 0x3fb8aa3b, v5
	v_ldexp_f32 v4, v9, v12
	v_fma_f32 v12, v5, s3, -v10
	v_rndne_f32_e32 v13, v10
	v_fmac_f32_e32 v12, 0x32a5705f, v5
	v_sub_f32_e32 v10, v10, v13
	v_add_f32_e32 v10, v10, v12
	v_exp_f32_e32 v10, v10
	v_cvt_i32_f32_e32 v12, v13
	ds_read2st64_b32 v[8:9], v8 offset0:4 offset1:6
	v_cmp_ngt_f32_e32 vcc, s4, v6
	s_nop 1
	v_cndmask_b32_e32 v4, 0, v4, vcc
	v_cmp_nlt_f32_e32 vcc, s5, v6
	v_ldexp_f32 v6, v10, v12
	s_nop 0
	v_cndmask_b32_e32 v4, v11, v4, vcc
	v_cmp_ngt_f32_e32 vcc, s4, v5
	s_waitcnt lgkmcnt(0)
	v_fmac_f32_e32 v14, v4, v8
	v_cndmask_b32_e32 v6, 0, v6, vcc
	v_cmp_nlt_f32_e32 vcc, s5, v5
	s_nop 1
	v_cndmask_b32_e32 v5, v11, v6, vcc
	s_lshl_b32 s36, s2, 2
	v_and_b32_e32 v6, 0x7c, v0
	v_lshl_or_b32 v6, v6, 8, s36
	v_and_or_b32 v6, v0, 3, v6
	v_fmac_f32_e32 v14, v5, v9
	v_lshl_add_u64 v[6:7], v[6:7], 2, s[20:21]
	global_store_dword v[6:7], v14, off
	s_and_b64 exec, exec, s[0:1]
	s_cbranch_execz .LBB0_81
	s_lshl_b32 s0, s2, 1
	s_mov_b32 s1, 0
	v_add_f32_e32 v0, v1, v3
	s_lshl_b64 s[0:1], s[0:1], 2
	v_add_f32_e32 v0, v0, v4
	s_add_u32 s0, s20, s0
	v_add_f32_e32 v3, v0, v5
	s_addc_u32 s1, s21, s1
	v_mov_b32_e32 v0, 0x20000
	global_store_dwordx2 v0, v[2:3], s[0:1]

_Z12pool3_kernelPKfS0_Pf:
	s_load_dwordx4 s[4:7], s[0:1], 0x0
	s_load_dwordx2 s[8:9], s[0:1], 0x10
	v_and_b32_e32 v1, 63, v0
	v_lshrrev_b32_e32 v2, 6, v0
	v_lshlrev_b32_e32 v3, 3, v1
	v_lshlrev_b32_e32 v4, 4, v1
	s_lshl_b32 s12, s2, 14
	s_lshl_b32 s13, s2, 6
	v_lshl_add_u32 v5, v2, 12, v4
	v_add_u32_e32 v5, s12, v5
	v_lshlrev_b32_e32 v6, 9, v1
	v_lshl_add_u32 v6, v2, 4, v6
	v_add_u32_e32 v6, s13, v6
	v_add_u32_e32 v7, 0x8000, v6
	v_lshlrev_b32_e32 v8, 2, v1
	s_waitcnt lgkmcnt(0)
	s_add_u32 s10, s4, 0x20000
	s_addc_u32 s11, s5, 0
	global_load_dwordx2 v[10:11], v3, s[10:11]
	global_load_dwordx2 v[12:13], v3, s[10:11] offset:512
	global_load_dwordx2 v[14:15], v3, s[10:11] offset:1024
	global_load_dwordx2 v[16:17], v3, s[10:11] offset:1536
	global_load_dwordx4 v[20:23], v5, s[4:5]
	global_load_dwordx4 v[24:27], v5, s[4:5] offset:1024
	global_load_dwordx4 v[28:31], v5, s[4:5] offset:2048
	global_load_dwordx4 v[32:35], v5, s[4:5] offset:3072
	global_load_dwordx4 v[36:39], v6, s[6:7]
	global_load_dwordx4 v[40:43], v7, s[6:7]
	s_waitcnt vmcnt(6)
	v_max_f32_e32 v44, v10, v12
	v_max_f32_e32 v45, v14, v16
	v_max_f32_e32 v44, v44, v45
	s_nop 1
	v_max_f32_dpp v44, v44, v44 row_shr:1 row_mask:0xf bank_mask:0xf
	s_nop 1
	v_max_f32_dpp v44, v44, v44 row_shr:2 row_mask:0xf bank_mask:0xf
	s_nop 1
	v_max_f32_dpp v44, v44, v44 row_shr:4 row_mask:0xf bank_mask:0xf
	s_nop 1
	v_max_f32_dpp v44, v44, v44 row_shr:8 row_mask:0xf bank_mask:0xf
	s_nop 1
	v_max_f32_dpp v44, v44, v44 row_bcast:15 row_mask:0xa bank_mask:0xf
	s_nop 1
	v_max_f32_dpp v44, v44, v44 row_bcast:31 row_mask:0xc bank_mask:0xf
	s_nop 1
	v_readlane_b32 s14, v44, 63
	s_nop 1
	v_subrev_f32_e32 v46, s14, v10
	v_subrev_f32_e32 v47, s14, v12
	v_subrev_f32_e32 v48, s14, v14
	v_subrev_f32_e32 v49, s14, v16
	v_mul_f32_e32 v46, 0x3fb8aa3b, v46
	v_mul_f32_e32 v47, 0x3fb8aa3b, v47
	v_mul_f32_e32 v48, 0x3fb8aa3b, v48
	v_mul_f32_e32 v49, 0x3fb8aa3b, v49
	v_exp_f32_e32 v46, v46
	v_exp_f32_e32 v47, v47
	v_exp_f32_e32 v48, v48
	v_exp_f32_e32 v49, v49
	s_nop 0
	v_mul_f32_e32 v50, v11, v46
	v_fmac_f32_e32 v50, v13, v47
	v_fmac_f32_e32 v50, v15, v48
	v_fmac_f32_e32 v50, v17, v49
	s_waitcnt vmcnt(2)
	v_mul_f32_e32 v52, v46, v20
	v_mul_f32_e32 v53, v46, v21
	v_mul_f32_e32 v54, v46, v22
	v_mul_f32_e32 v55, v46, v23
	v_fmac_f32_e32 v52, v47, v24
	v_fmac_f32_e32 v53, v47, v25
	v_fmac_f32_e32 v54, v47, v26
	v_fmac_f32_e32 v55, v47, v27
	v_fmac_f32_e32 v52, v48, v28
	v_fmac_f32_e32 v53, v48, v29
	v_fmac_f32_e32 v54, v48, v30
	v_fmac_f32_e32 v55, v48, v31
	v_fmac_f32_e32 v52, v49, v32
	v_fmac_f32_e32 v53, v49, v33
	v_fmac_f32_e32 v54, v49, v34
	v_fmac_f32_e32 v55, v49, v35
	v_add_f32_dpp v50, v50, v50 row_shr:1 row_mask:0xf bank_mask:0xf
	v_add_f32_dpp v52, v52, v52 row_shr:1 row_mask:0xf bank_mask:0xf
	v_add_f32_dpp v53, v53, v53 row_shr:1 row_mask:0xf bank_mask:0xf
	v_add_f32_dpp v54, v54, v54 row_shr:1 row_mask:0xf bank_mask:0xf
	v_add_f32_dpp v55, v55, v55 row_shr:1 row_mask:0xf bank_mask:0xf
	v_add_f32_dpp v50, v50, v50 row_shr:2 row_mask:0xf bank_mask:0xf
	v_add_f32_dpp v52, v52, v52 row_shr:2 row_mask:0xf bank_mask:0xf
	v_add_f32_dpp v53, v53, v53 row_shr:2 row_mask:0xf bank_mask:0xf
	v_add_f32_dpp v54, v54, v54 row_shr:2 row_mask:0xf bank_mask:0xf
	v_add_f32_dpp v55, v55, v55 row_shr:2 row_mask:0xf bank_mask:0xf
	v_add_f32_dpp v50, v50, v50 row_shr:4 row_mask:0xf bank_mask:0xf
	v_add_f32_dpp v52, v52, v52 row_shr:4 row_mask:0xf bank_mask:0xf
	v_add_f32_dpp v53, v53, v53 row_shr:4 row_mask:0xf bank_mask:0xf
	v_add_f32_dpp v54, v54, v54 row_shr:4 row_mask:0xf bank_mask:0xf
	v_add_f32_dpp v55, v55, v55 row_shr:4 row_mask:0xf bank_mask:0xf
	v_add_f32_dpp v50, v50, v50 row_shr:8 row_mask:0xf bank_mask:0xf
	v_add_f32_dpp v52, v52, v52 row_shr:8 row_mask:0xf bank_mask:0xf
	v_add_f32_dpp v53, v53, v53 row_shr:8 row_mask:0xf bank_mask:0xf
	v_add_f32_dpp v54, v54, v54 row_shr:8 row_mask:0xf bank_mask:0xf
	v_add_f32_dpp v55, v55, v55 row_shr:8 row_mask:0xf bank_mask:0xf
	v_add_f32_dpp v50, v50, v50 row_bcast:15 row_mask:0xa bank_mask:0xf
	v_add_f32_dpp v52, v52, v52 row_bcast:15 row_mask:0xa bank_mask:0xf
	v_add_f32_dpp v53, v53, v53 row_bcast:15 row_mask:0xa bank_mask:0xf
	v_add_f32_dpp v54, v54, v54 row_bcast:15 row_mask:0xa bank_mask:0xf
	v_add_f32_dpp v55, v55, v55 row_bcast:15 row_mask:0xa bank_mask:0xf
	v_add_f32_dpp v50, v50, v50 row_bcast:31 row_mask:0xc bank_mask:0xf
	v_add_f32_dpp v52, v52, v52 row_bcast:31 row_mask:0xc bank_mask:0xf
	v_add_f32_dpp v53, v53, v53 row_bcast:31 row_mask:0xc bank_mask:0xf
	v_add_f32_dpp v54, v54, v54 row_bcast:31 row_mask:0xc bank_mask:0xf
	v_add_f32_dpp v55, v55, v55 row_bcast:31 row_mask:0xc bank_mask:0xf
	s_nop 1
	v_readlane_b32 s15, v50, 63
	v_readlane_b32 s16, v52, 63
	v_readlane_b32 s17, v53, 63
	v_readlane_b32 s18, v54, 63
	v_readlane_b32 s19, v55, 63
	s_nop 1
	v_mov_b32_e32 v56, s15
	v_rcp_f32_e32 v56, v56
	s_nop 0
	v_mul_f32_e32 v57, s16, v56
	v_mul_f32_e32 v58, s17, v56
	v_mul_f32_e32 v59, s18, v56
	v_mul_f32_e32 v60, s19, v56
	s_waitcnt vmcnt(0)
	v_mul_f32_e32 v61, v36, v57
	v_mul_f32_e32 v62, v40, v57
	v_fmac_f32_e32 v61, v37, v58
	v_fmac_f32_e32 v62, v41, v58
	v_fmac_f32_e32 v61, v38, v59
	v_fmac_f32_e32 v62, v42, v59
	v_fmac_f32_e32 v61, v39, v60
	v_fmac_f32_e32 v62, v43, v60
	v_lshl_add_u32 v9, v2, 9, v8
	ds_write_b32 v9, v61
	ds_write_b32 v9, v62 offset:256
	v_readfirstlane_b32 s20, v2
	s_waitcnt lgkmcnt(0)
	s_barrier
	s_cmp_lg_u32 s20, 0
	s_cbranch_scc1 .Lp3_done
	ds_read_b32 v61, v8
	ds_read_b32 v62, v8 offset:256
	ds_read_b32 v52, v8 offset:512
	ds_read_b32 v53, v8 offset:768
	ds_read_b32 v54, v8 offset:1024
	ds_read_b32 v55, v8 offset:1280
	ds_read_b32 v56, v8 offset:1536
	ds_read_b32 v57, v8 offset:1792
	s_waitcnt lgkmcnt(4)
	v_add_f32_e32 v61, v61, v52
	v_add_f32_e32 v62, v62, v53
	s_waitcnt lgkmcnt(2)
	v_add_f32_e32 v61, v61, v54
	v_add_f32_e32 v62, v62, v55
	s_waitcnt lgkmcnt(0)
	v_add_f32_e32 v61, v61, v56
	v_add_f32_e32 v62, v62, v57
	global_atomic_add_f32 v8, v61, s[8:9]
	global_atomic_add_f32 v8, v62, s[8:9] offset:256
